# gelu quads of the RG in-projection epilogue packed (v_pk_mul/fma/add_f32): phase probe -1.6 us per execution
# speedup vs baseline: 1.0026x; 1.0026x over previous
; __device__ __forceinline__ void rows_rs(const float* ssq, int row0, int fq, float (&rs)[2][4]) {
;     f32x4 p[2][4];
; #pragma unroll
;     for (int ai = 0; ai < 2; ++ai)
; #pragma unroll
;         for (int m = 0; m < 4; ++m) p[ai][m] = *(const f32x4*)(ssq + (size_t)(row0 + ai * 128 + m * 16) * 16 + 4 * fq);
; #pragma unroll
;     for (int ai = 0; ai < 2; ++ai)
; #pragma unroll
;         for (int m = 0; m < 4; ++m) { float s = (p[ai][m][0] + p[ai][m][1]) + (p[ai][m][2] + p[ai][m][3]); s += __shfl_xor(s, 16); s += __shfl_xor(s, 32); rs[ai][m] = rsqrtf(s * (1.f / D) + EPS); }
; }
; template <bool FP8>
; __device__ __forceinline__ void epilogue(const Desc& d, const Acc& acc, const Tile& u, LAS unsigned char* lds) {
;     ...
;         const int row0 = u.pm * 256 + lr0, col0 = u.pn * 256 + lc0; const bool isg = u.pn < 4;
;         bf16* O = isg ? (bf16*)d.o0 : (bf16*)d.o1; const int oc0 = isg ? col0 : col0 - 1024; const float* bias = (const float*)d.p0; const float* ssq = (const float*)d.p1;
;         float rs[2][4]; f32x4 bv[2][2];
;         rows_rs(ssq, row0, fq, rs);
; #pragma unroll
;         for (int bj = 0; bj < 2; ++bj)
; #pragma unroll
;             for (int n = 0; n < 2; ++n) bv[bj][n] = *(const f32x4*)(bias + col0 + bj * 128 + n * 4);
; #pragma unroll
;         for (int ai = 0; ai < 2; ++ai)
; #pragma unroll
;             for (int m = 0; m < 4; ++m)
; #pragma unroll
;                 for (int bj = 0; bj < 2; ++bj) { f32x4 v[2];
; #pragma unroll
;                     for (int n = 0; n < 2; ++n) { v[n] = acc[ai][bj][m][n] * rs[ai][m] + bv[bj][n];
;                         if (isg) { v[n][0] = gelu_tanh(v[n][0]); v[n][1] = gelu_tanh(v[n][1]); v[n][2] = gelu_tanh(v[n][2]); v[n][3] = gelu_tanh(v[n][3]); } }
.LBB0_557:
	s_and_b64 vcc, exec, s[6:7]
	s_cbranch_vccz .LBB0_623
	v_lshl_add_u32 v176, s44, 8, v194
	v_or_b32_e32 v172, 16, v176
	v_lshlrev_b32_e32 v66, 4, v222
	v_ashrrev_i32_e32 v177, 31, v176
	v_ashrrev_i32_e32 v173, 31, v172
	v_lshl_add_u64 v[168:169], s[56:57], 0, v[66:67]
	v_lshlrev_b64 v[132:133], 6, v[176:177]
	v_lshlrev_b64 v[136:137], 6, v[172:173]
	v_lshl_add_u64 v[132:133], v[168:169], 0, v[132:133]
	v_lshl_add_u64 v[136:137], v[168:169], 0, v[136:137]
	global_load_dwordx4 v[132:135], v[132:133], off
	v_or_b32_e32 v166, 32, v176
	global_load_dwordx4 v[136:139], v[136:137], off
	v_or_b32_e32 v164, 48, v176
	v_ashrrev_i32_e32 v167, 31, v166
	v_ashrrev_i32_e32 v165, 31, v164
	v_lshlrev_b64 v[140:141], 6, v[166:167]
	v_lshlrev_b64 v[144:145], 6, v[164:165]
	v_lshl_add_u64 v[140:141], v[168:169], 0, v[140:141]
	v_lshl_add_u64 v[144:145], v[168:169], 0, v[144:145]
	global_load_dwordx4 v[140:143], v[140:141], off
	v_add_u32_e32 v158, 0x80, v176
	global_load_dwordx4 v[144:147], v[144:145], off
	v_ashrrev_i32_e32 v159, 31, v158
	v_lshlrev_b64 v[148:149], 6, v[158:159]
	v_add_u32_e32 v156, 0x90, v176
	v_lshl_add_u64 v[148:149], v[168:169], 0, v[148:149]
	v_ashrrev_i32_e32 v157, 31, v156
	global_load_dwordx4 v[152:155], v[148:149], off
	v_lshlrev_b64 v[148:149], 6, v[156:157]
	v_lshl_add_u64 v[148:149], v[168:169], 0, v[148:149]
	global_load_dwordx4 v[160:163], v[148:149], off
	v_add_u32_e32 v150, 0xa0, v176
	v_ashrrev_i32_e32 v151, 31, v150
	v_lshlrev_b64 v[148:149], 6, v[150:151]
	v_lshl_add_u64 v[148:149], v[168:169], 0, v[148:149]
	v_lshl_or_b32 v178, s88, 8, v200
	global_load_dwordx4 v[198:201], v[148:149], off
	v_add_u32_e32 v148, 0xb0, v176
	v_ashrrev_i32_e32 v149, 31, v148
	v_lshlrev_b64 v[170:171], 6, v[148:149]
	v_lshl_add_u64 v[168:169], v[168:169], 0, v[170:171]
	global_load_dwordx4 v[202:205], v[168:169], off
	v_cmp_lt_i32_e32 vcc, v249, v240
	s_mov_b32 s2, 0x3a800000
	s_cmp_lt_i32 s88, 4
	v_cndmask_b32_e32 v66, v238, v249, vcc
	v_cmp_lt_i32_e32 vcc, v246, v240
	v_lshlrev_b32_e32 v66, 2, v66
	s_cselect_b64 s[44:45], -1, 0
	v_cndmask_b32_e32 v168, v238, v246, vcc
	v_lshlrev_b32_e32 v179, 2, v168
	s_cmp_gt_i32 s88, 3
	s_waitcnt vmcnt(0)
	v_mov_b32_e32 v168, v133
	v_mov_b32_e32 v169, v134
	v_mov_b32_e32 v133, v135
	v_mov_b32_e32 v134, v137
	v_mov_b32_e32 v135, v138
	v_mov_b32_e32 v137, v139
	v_pk_add_f32 v[132:133], v[168:169], v[132:133]
	v_pk_add_f32 v[134:135], v[134:135], v[136:137]
	v_mov_b32_e32 v137, v132
	v_mov_b32_e32 v136, v134
	v_mov_b32_e32 v132, v135
	v_pk_add_f32 v[132:133], v[136:137], v[132:133]
	ds_bpermute_b32 v135, v66, v133
	ds_bpermute_b32 v134, v66, v132
	s_waitcnt lgkmcnt(0)
	v_pk_add_f32 v[132:133], v[132:133], v[134:135]
	ds_bpermute_b32 v135, v179, v133
	ds_bpermute_b32 v134, v179, v132
	s_waitcnt lgkmcnt(0)
	v_pk_add_f32 v[132:133], v[132:133], v[134:135]
	s_nop 0
	v_pk_fma_f32 v[174:175], v[132:133], s[2:3], v[196:197] op_sel_hi:[1,0,0]
	v_mov_b32_e32 v134, v145
	v_mul_f32_e32 v132, 0x4b800000, v175
	v_cmp_gt_f32_e32 vcc, s39, v175
	v_mov_b32_e32 v135, v146
	v_mov_b32_e32 v145, v147
	v_cndmask_b32_e32 v132, v175, v132, vcc
	v_rsq_f32_e32 v132, v132
	v_pk_add_f32 v[134:135], v[134:135], v[144:145]
	v_cmp_gt_f32_e64 s[42:43], s39, v174
	v_mov_b32_e32 v136, v134
	v_mul_f32_e32 v133, 0x45800000, v132
	v_cndmask_b32_e32 v194, v132, v133, vcc
	v_mov_b32_e32 v132, v141
	v_mov_b32_e32 v133, v142
	v_mov_b32_e32 v141, v143
	v_pk_add_f32 v[132:133], v[132:133], v[140:141]
	s_nop 0
	v_mov_b32_e32 v137, v132
	v_mov_b32_e32 v132, v135
	v_pk_add_f32 v[132:133], v[136:137], v[132:133]
	ds_bpermute_b32 v135, v66, v133
	ds_bpermute_b32 v134, v66, v132
	s_waitcnt lgkmcnt(0)
	v_pk_add_f32 v[168:169], v[132:133], v[134:135]
	v_mov_b32_e32 v132, v153
	v_mov_b32_e32 v133, v154
	v_mov_b32_e32 v153, v155
	v_mov_b32_e32 v134, v161
	v_mov_b32_e32 v135, v162
	v_mov_b32_e32 v161, v163
	v_pk_add_f32 v[132:133], v[132:133], v[152:153]
	v_pk_add_f32 v[134:135], v[134:135], v[160:161]
	v_mov_b32_e32 v137, v132
	v_mov_b32_e32 v136, v134
	v_mov_b32_e32 v132, v135
	v_pk_add_f32 v[132:133], v[136:137], v[132:133]
	ds_bpermute_b32 v135, v66, v133
	ds_bpermute_b32 v134, v66, v132
	ds_bpermute_b32 v171, v179, v169
	ds_bpermute_b32 v170, v179, v168
	s_waitcnt lgkmcnt(2)
	v_pk_add_f32 v[160:161], v[132:133], v[134:135]
	v_mov_b32_e32 v132, v199
	v_mov_b32_e32 v133, v200
	v_mov_b32_e32 v199, v201
	v_mov_b32_e32 v134, v203
	v_mov_b32_e32 v135, v204
	v_mov_b32_e32 v203, v205
	v_pk_add_f32 v[132:133], v[132:133], v[198:199]
	v_pk_add_f32 v[134:135], v[134:135], v[202:203]
	v_mov_b32_e32 v137, v132
	v_mov_b32_e32 v136, v134
	v_mov_b32_e32 v132, v135
	v_pk_add_f32 v[132:133], v[136:137], v[132:133]
	ds_bpermute_b32 v135, v66, v133
	ds_bpermute_b32 v134, v66, v132
	ds_bpermute_b32 v163, v179, v161
	ds_bpermute_b32 v162, v179, v160
	s_waitcnt lgkmcnt(2)
	v_pk_add_f32 v[152:153], v[132:133], v[134:135]
	ds_bpermute_b32 v155, v179, v153
	ds_bpermute_b32 v154, v179, v152
	v_ashrrev_i32_e32 v179, 31, v178
	v_lshl_add_u64 v[136:137], v[178:179], 2, s[54:55]
	global_load_dwordx4 v[140:143], v[136:137], off offset:16
	global_load_dwordx4 v[144:147], v[136:137], off
	global_load_dwordx4 v[132:135], v[136:137], off offset:528
	s_nop 0
	global_load_dwordx4 v[136:139], v[136:137], off offset:512
	s_waitcnt vmcnt(2)
	v_pk_fma_f32 v[130:131], v[130:131], v[194:195], v[146:147] op_sel_hi:[1,0,1]
	v_pk_fma_f32 v[128:129], v[128:129], v[194:195], v[144:145] op_sel_hi:[1,0,1]
	s_cbranch_scc1 .LBB0_560
	v_mov_b32_e32 v210, 0x3dd2d3e7
	v_pk_mul_f32 v[206:207], v[128:129], v[128:129]
	v_pk_mul_f32 v[208:209], v[130:131], v[130:131]
	v_pk_fma_f32 v[206:207], v[206:207], v[210:211], v[236:237] op_sel_hi:[1,0,0]
	v_pk_fma_f32 v[208:209], v[208:209], v[210:211], v[236:237] op_sel_hi:[1,0,0]
	v_pk_mul_f32 v[206:207], v[128:129], v[206:207]
	v_pk_mul_f32 v[208:209], v[130:131], v[208:209]
	v_exp_f32_e32 v206, v206
	v_exp_f32_e32 v207, v207
	v_exp_f32_e32 v208, v208
	v_exp_f32_e32 v209, v209
	v_pk_add_f32 v[206:207], v[206:207], 1.0 op_sel_hi:[1,0]
	v_pk_add_f32 v[208:209], v[208:209], 1.0 op_sel_hi:[1,0]
	v_rcp_f32_e32 v206, v206
	v_rcp_f32_e32 v207, v207
	v_rcp_f32_e32 v208, v208
	v_rcp_f32_e32 v209, v209
	v_pk_fma_f32 v[128:129], v[128:129], v[206:207], v[128:129] neg_lo:[1,0,0] neg_hi:[1,0,0]
	v_pk_fma_f32 v[130:131], v[130:131], v[208:209], v[130:131] neg_lo:[1,0,0] neg_hi:[1,0,0]
; __device__ __forceinline__ void store_bf16x8_wt(bf16* p, const f32x4 v0, const f32x4 v1) { u32x4 w; w.x = cvt_pk_bf16(v0[0], v0[1]); w.y = cvt_pk_bf16(v0[2], v0[3]); w.z = cvt_pk_bf16(v1[0], v1[1]); w.w = cvt_pk_bf16(v1[2], v1[3]); stg16_wt(p, w); }
; __device__ __forceinline__ float gelu_tanh(float x) {
;     const float C0 = 2.f * 0.7978845608028654f * L2E, C1 = 2.f * 0.7978845608028654f * 0.044715f * L2E;
;     const float e = __builtin_amdgcn_exp2f(x * __builtin_fmaf(x * x, C1, C0));
;     return __builtin_fmaf(-x, __builtin_amdgcn_rcpf(1.f + e), x);
; }
; template <bool FP8>
; __device__ __forceinline__ void epilogue(const Desc& d, const Acc& acc, const Tile& u, LAS unsigned char* lds) {
;     ...
;         for (int ai = 0; ai < 2; ++ai)
; #pragma unroll
;             for (int m = 0; m < 4; ++m)
; #pragma unroll
;                 for (int bj = 0; bj < 2; ++bj) { f32x4 v[2];
; #pragma unroll
;                     for (int n = 0; n < 2; ++n) { v[n] = acc[ai][bj][m][n] * rs[ai][m] + bv[bj][n];
;                         if (isg) { v[n][0] = gelu_tanh(v[n][0]); v[n][1] = gelu_tanh(v[n][1]); v[n][2] = gelu_tanh(v[n][2]); v[n][3] = gelu_tanh(v[n][3]); } }
;                     store_bf16x8_wt(O + (size_t)(row0 + ai * 128 + m * 16) * D + oc0 + bj * 128, v[0], v[1]); }
.LBB0_560:
	v_mov_b32_e32 v195, v194
	v_mov_b32_e32 v200, v194
	v_mov_b32_e32 v201, v194
	v_cndmask_b32_e64 v66, 0, 1, s[44:45]
	v_pk_fma_f32 v[202:203], v[126:127], v[200:201], v[142:143]
	v_cmp_ne_u32_e64 s[40:41], 1, v66
	s_andn2_b64 vcc, exec, s[44:45]
	v_pk_fma_f32 v[204:205], v[124:125], v[194:195], v[140:141]
	s_cbranch_vccnz .LBB0_562
	v_mov_b32_e32 v210, 0x3dd2d3e7
	v_pk_mul_f32 v[206:207], v[204:205], v[204:205]
	v_pk_mul_f32 v[208:209], v[202:203], v[202:203]
	v_pk_fma_f32 v[206:207], v[206:207], v[210:211], v[236:237] op_sel_hi:[1,0,0]
	v_pk_fma_f32 v[208:209], v[208:209], v[210:211], v[236:237] op_sel_hi:[1,0,0]
	v_pk_mul_f32 v[206:207], v[204:205], v[206:207]
	v_pk_mul_f32 v[208:209], v[202:203], v[208:209]
	v_exp_f32_e32 v206, v206
	v_exp_f32_e32 v207, v207
	v_exp_f32_e32 v208, v208
	v_exp_f32_e32 v209, v209
	v_pk_add_f32 v[206:207], v[206:207], 1.0 op_sel_hi:[1,0]
	v_pk_add_f32 v[208:209], v[208:209], 1.0 op_sel_hi:[1,0]
	v_rcp_f32_e32 v206, v206
	v_rcp_f32_e32 v207, v207
	v_rcp_f32_e32 v208, v208
	v_rcp_f32_e32 v209, v209
	v_pk_fma_f32 v[204:205], v[204:205], v[206:207], v[204:205] neg_lo:[1,0,0] neg_hi:[1,0,0]
	v_pk_fma_f32 v[202:203], v[202:203], v[208:209], v[202:203] neg_lo:[1,0,0] neg_hi:[1,0,0]
.LBB0_562:
	s_and_b64 s[6:7], s[44:45], exec
	v_add_u32_e32 v66, 0xfffffc00, v178
	s_cselect_b32 s2, s51, s73
	s_cselect_b32 s6, s50, s72
	v_cndmask_b32_e64 v126, v66, v178, s[44:45]
	v_mov_b32_e32 v124, s6
	v_mov_b32_e32 v125, s2
	v_ashrrev_i32_e32 v127, 31, v126
	v_lshl_add_u64 v[124:125], v[126:127], 1, v[124:125]
	v_lshlrev_b64 v[126:127], 11, v[176:177]
	v_lshl_add_u64 v[126:127], v[124:125], 0, v[126:127]
	v_cvt_pk_bf16_f32 v128, v128, v129
	v_cvt_pk_bf16_f32 v129, v130, v131
	v_cvt_pk_bf16_f32 v130, v204, v205
	v_cvt_pk_bf16_f32 v131, v202, v203
	s_waitcnt vmcnt(0)
	v_pk_fma_f32 v[122:123], v[122:123], v[200:201], v[138:139]
	global_store_dwordx4 v[126:127], v[128:131], off sc1
	s_nop 1
	s_and_b64 vcc, exec, s[40:41]
	v_pk_fma_f32 v[120:121], v[120:121], v[194:195], v[136:137]
	s_cbranch_vccnz .LBB0_564
	v_mov_b32_e32 v210, 0x3dd2d3e7
	v_pk_mul_f32 v[206:207], v[120:121], v[120:121]
	v_pk_mul_f32 v[208:209], v[122:123], v[122:123]
	v_pk_fma_f32 v[206:207], v[206:207], v[210:211], v[236:237] op_sel_hi:[1,0,0]
	v_pk_fma_f32 v[208:209], v[208:209], v[210:211], v[236:237] op_sel_hi:[1,0,0]
	v_pk_mul_f32 v[206:207], v[120:121], v[206:207]
	v_pk_mul_f32 v[208:209], v[122:123], v[208:209]
	v_exp_f32_e32 v206, v206
	v_exp_f32_e32 v207, v207
	v_exp_f32_e32 v208, v208
	v_exp_f32_e32 v209, v209
	v_pk_add_f32 v[206:207], v[206:207], 1.0 op_sel_hi:[1,0]
	v_pk_add_f32 v[208:209], v[208:209], 1.0 op_sel_hi:[1,0]
	v_rcp_f32_e32 v206, v206
	v_rcp_f32_e32 v207, v207
	v_rcp_f32_e32 v208, v208
	v_rcp_f32_e32 v209, v209
	v_pk_fma_f32 v[120:121], v[120:121], v[206:207], v[120:121] neg_lo:[1,0,0] neg_hi:[1,0,0]
	v_pk_fma_f32 v[122:123], v[122:123], v[208:209], v[122:123] neg_lo:[1,0,0] neg_hi:[1,0,0]
.LBB0_564:
	v_mov_b32_e32 v128, v194
	v_mov_b32_e32 v129, v194
	v_pk_fma_f32 v[118:119], v[118:119], v[128:129], v[134:135]
	s_and_b64 vcc, exec, s[40:41]
	v_pk_fma_f32 v[128:129], v[116:117], v[194:195], v[132:133]
	s_cbranch_vccnz .LBB0_566
	v_mov_b32_e32 v210, 0x3dd2d3e7
	v_pk_mul_f32 v[206:207], v[128:129], v[128:129]
	v_pk_mul_f32 v[208:209], v[118:119], v[118:119]
	v_pk_fma_f32 v[206:207], v[206:207], v[210:211], v[236:237] op_sel_hi:[1,0,0]
	v_pk_fma_f32 v[208:209], v[208:209], v[210:211], v[236:237] op_sel_hi:[1,0,0]
	v_pk_mul_f32 v[206:207], v[128:129], v[206:207]
	v_pk_mul_f32 v[208:209], v[118:119], v[208:209]
	v_exp_f32_e32 v206, v206
	v_exp_f32_e32 v207, v207
	v_exp_f32_e32 v208, v208
	v_exp_f32_e32 v209, v209
	v_pk_add_f32 v[206:207], v[206:207], 1.0 op_sel_hi:[1,0]
	v_pk_add_f32 v[208:209], v[208:209], 1.0 op_sel_hi:[1,0]
	v_rcp_f32_e32 v206, v206
	v_rcp_f32_e32 v207, v207
	v_rcp_f32_e32 v208, v208
	v_rcp_f32_e32 v209, v209
	v_pk_fma_f32 v[128:129], v[128:129], v[206:207], v[128:129] neg_lo:[1,0,0] neg_hi:[1,0,0]
	v_pk_fma_f32 v[118:119], v[118:119], v[208:209], v[118:119] neg_lo:[1,0,0] neg_hi:[1,0,0]
.LBB0_566:
	v_mul_f32_e32 v66, 0x4b800000, v174
	v_cndmask_b32_e64 v66, v174, v66, s[42:43]
	v_rsq_f32_e32 v66, v66
	v_lshl_add_u64 v[126:127], v[126:127], 0, s[4:5]
	v_cvt_pk_bf16_f32 v120, v120, v121
	v_cvt_pk_bf16_f32 v121, v122, v123
	v_mul_f32_e32 v116, 0x45800000, v66
	v_cvt_pk_bf16_f32 v122, v128, v129
	v_cvt_pk_bf16_f32 v123, v118, v119
	v_cndmask_b32_e64 v116, v66, v116, s[42:43]
	global_store_dwordx4 v[126:127], v[120:123], off sc1
	s_nop 1
	v_pk_fma_f32 v[114:115], v[114:115], v[116:117], v[146:147] op_sel_hi:[1,0,1]
	s_and_b64 vcc, exec, s[40:41]
	v_pk_fma_f32 v[112:113], v[112:113], v[116:117], v[144:145] op_sel_hi:[1,0,1]
	s_cbranch_vccnz .LBB0_568
	v_mov_b32_e32 v210, 0x3dd2d3e7
	v_pk_mul_f32 v[206:207], v[112:113], v[112:113]
	v_pk_mul_f32 v[208:209], v[114:115], v[114:115]
	v_pk_fma_f32 v[206:207], v[206:207], v[210:211], v[236:237] op_sel_hi:[1,0,0]
	v_pk_fma_f32 v[208:209], v[208:209], v[210:211], v[236:237] op_sel_hi:[1,0,0]
	v_pk_mul_f32 v[206:207], v[112:113], v[206:207]
	v_pk_mul_f32 v[208:209], v[114:115], v[208:209]
	v_exp_f32_e32 v206, v206
	v_exp_f32_e32 v207, v207
	v_exp_f32_e32 v208, v208
	v_exp_f32_e32 v209, v209
	v_pk_add_f32 v[206:207], v[206:207], 1.0 op_sel_hi:[1,0]
	v_pk_add_f32 v[208:209], v[208:209], 1.0 op_sel_hi:[1,0]
	v_rcp_f32_e32 v206, v206
	v_rcp_f32_e32 v207, v207
	v_rcp_f32_e32 v208, v208
	v_rcp_f32_e32 v209, v209
	v_pk_fma_f32 v[112:113], v[112:113], v[206:207], v[112:113] neg_lo:[1,0,0] neg_hi:[1,0,0]
	v_pk_fma_f32 v[114:115], v[114:115], v[208:209], v[114:115] neg_lo:[1,0,0] neg_hi:[1,0,0]
; __device__ __forceinline__ void store_bf16x8_wt(bf16* p, const f32x4 v0, const f32x4 v1) { u32x4 w; w.x = cvt_pk_bf16(v0[0], v0[1]); w.y = cvt_pk_bf16(v0[2], v0[3]); w.z = cvt_pk_bf16(v1[0], v1[1]); w.w = cvt_pk_bf16(v1[2], v1[3]); stg16_wt(p, w); }
; __device__ __forceinline__ float gelu_tanh(float x) {
;     const float C0 = 2.f * 0.7978845608028654f * L2E, C1 = 2.f * 0.7978845608028654f * 0.044715f * L2E;
;     const float e = __builtin_amdgcn_exp2f(x * __builtin_fmaf(x * x, C1, C0));
;     return __builtin_fmaf(-x, __builtin_amdgcn_rcpf(1.f + e), x);
; }
; template <bool FP8>
; __device__ __forceinline__ void epilogue(const Desc& d, const Acc& acc, const Tile& u, LAS unsigned char* lds) {
;     ...
;         for (int ai = 0; ai < 2; ++ai)
; #pragma unroll
;             for (int m = 0; m < 4; ++m)
; #pragma unroll
;                 for (int bj = 0; bj < 2; ++bj) { f32x4 v[2];
; #pragma unroll
;                     for (int n = 0; n < 2; ++n) { v[n] = acc[ai][bj][m][n] * rs[ai][m] + bv[bj][n];
;                         if (isg) { v[n][0] = gelu_tanh(v[n][0]); v[n][1] = gelu_tanh(v[n][1]); v[n][2] = gelu_tanh(v[n][2]); v[n][3] = gelu_tanh(v[n][3]); } }
;                     store_bf16x8_wt(O + (size_t)(row0 + ai * 128 + m * 16) * D + oc0 + bj * 128, v[0], v[1]); }
.LBB0_568:
	v_mov_b32_e32 v117, v116
	v_mov_b32_e32 v118, v116
	v_mov_b32_e32 v119, v116
	v_pk_fma_f32 v[110:111], v[110:111], v[118:119], v[142:143]
	s_and_b64 vcc, exec, s[40:41]
	v_pk_fma_f32 v[120:121], v[108:109], v[116:117], v[140:141]
	s_cbranch_vccnz .LBB0_570
	v_mov_b32_e32 v210, 0x3dd2d3e7
	v_pk_mul_f32 v[206:207], v[120:121], v[120:121]
	v_pk_mul_f32 v[208:209], v[110:111], v[110:111]
	v_pk_fma_f32 v[206:207], v[206:207], v[210:211], v[236:237] op_sel_hi:[1,0,0]
	v_pk_fma_f32 v[208:209], v[208:209], v[210:211], v[236:237] op_sel_hi:[1,0,0]
	v_pk_mul_f32 v[206:207], v[120:121], v[206:207]
	v_pk_mul_f32 v[208:209], v[110:111], v[208:209]
	v_exp_f32_e32 v206, v206
	v_exp_f32_e32 v207, v207
	v_exp_f32_e32 v208, v208
	v_exp_f32_e32 v209, v209
	v_pk_add_f32 v[206:207], v[206:207], 1.0 op_sel_hi:[1,0]
	v_pk_add_f32 v[208:209], v[208:209], 1.0 op_sel_hi:[1,0]
	v_rcp_f32_e32 v206, v206
	v_rcp_f32_e32 v207, v207
	v_rcp_f32_e32 v208, v208
	v_rcp_f32_e32 v209, v209
	v_pk_fma_f32 v[120:121], v[120:121], v[206:207], v[120:121] neg_lo:[1,0,0] neg_hi:[1,0,0]
	v_pk_fma_f32 v[110:111], v[110:111], v[208:209], v[110:111] neg_lo:[1,0,0] neg_hi:[1,0,0]
.LBB0_570:
	v_lshlrev_b64 v[108:109], 11, v[172:173]
	v_lshl_add_u64 v[108:109], v[124:125], 0, v[108:109]
	v_cvt_pk_bf16_f32 v112, v112, v113
	v_cvt_pk_bf16_f32 v113, v114, v115
	v_cvt_pk_bf16_f32 v114, v120, v121
	v_cvt_pk_bf16_f32 v115, v110, v111
	v_pk_fma_f32 v[106:107], v[106:107], v[118:119], v[138:139]
	global_store_dwordx4 v[108:109], v[112:115], off sc1
	s_nop 1
	s_and_b64 vcc, exec, s[40:41]
	v_pk_fma_f32 v[104:105], v[104:105], v[116:117], v[136:137]
	s_cbranch_vccnz .LBB0_572
	v_mov_b32_e32 v210, 0x3dd2d3e7
	v_pk_mul_f32 v[206:207], v[104:105], v[104:105]
	v_pk_mul_f32 v[208:209], v[106:107], v[106:107]
	v_pk_fma_f32 v[206:207], v[206:207], v[210:211], v[236:237] op_sel_hi:[1,0,0]
	v_pk_fma_f32 v[208:209], v[208:209], v[210:211], v[236:237] op_sel_hi:[1,0,0]
	v_pk_mul_f32 v[206:207], v[104:105], v[206:207]
	v_pk_mul_f32 v[208:209], v[106:107], v[208:209]
	v_exp_f32_e32 v206, v206
	v_exp_f32_e32 v207, v207
	v_exp_f32_e32 v208, v208
	v_exp_f32_e32 v209, v209
	v_pk_add_f32 v[206:207], v[206:207], 1.0 op_sel_hi:[1,0]
	v_pk_add_f32 v[208:209], v[208:209], 1.0 op_sel_hi:[1,0]
	v_rcp_f32_e32 v206, v206
	v_rcp_f32_e32 v207, v207
	v_rcp_f32_e32 v208, v208
	v_rcp_f32_e32 v209, v209
	v_pk_fma_f32 v[104:105], v[104:105], v[206:207], v[104:105] neg_lo:[1,0,0] neg_hi:[1,0,0]
	v_pk_fma_f32 v[106:107], v[106:107], v[208:209], v[106:107] neg_lo:[1,0,0] neg_hi:[1,0,0]
.LBB0_572:
	v_mov_b32_e32 v110, v116
	v_mov_b32_e32 v111, v116
	v_pk_fma_f32 v[110:111], v[102:103], v[110:111], v[134:135]
	s_and_b64 vcc, exec, s[40:41]
	v_pk_fma_f32 v[112:113], v[100:101], v[116:117], v[132:133]
	s_cbranch_vccnz .LBB0_574
	v_mov_b32_e32 v210, 0x3dd2d3e7
	v_pk_mul_f32 v[206:207], v[112:113], v[112:113]
	v_pk_mul_f32 v[208:209], v[110:111], v[110:111]
	v_pk_fma_f32 v[206:207], v[206:207], v[210:211], v[236:237] op_sel_hi:[1,0,0]
	v_pk_fma_f32 v[208:209], v[208:209], v[210:211], v[236:237] op_sel_hi:[1,0,0]
	v_pk_mul_f32 v[206:207], v[112:113], v[206:207]
	v_pk_mul_f32 v[208:209], v[110:111], v[208:209]
	v_exp_f32_e32 v206, v206
	v_exp_f32_e32 v207, v207
	v_exp_f32_e32 v208, v208
	v_exp_f32_e32 v209, v209
	v_pk_add_f32 v[206:207], v[206:207], 1.0 op_sel_hi:[1,0]
	v_pk_add_f32 v[208:209], v[208:209], 1.0 op_sel_hi:[1,0]
	v_rcp_f32_e32 v206, v206
	v_rcp_f32_e32 v207, v207
	v_rcp_f32_e32 v208, v208
	v_rcp_f32_e32 v209, v209
	v_pk_fma_f32 v[112:113], v[112:113], v[206:207], v[112:113] neg_lo:[1,0,0] neg_hi:[1,0,0]
	v_pk_fma_f32 v[110:111], v[110:111], v[208:209], v[110:111] neg_lo:[1,0,0] neg_hi:[1,0,0]
.LBB0_574:
	v_pk_add_f32 v[100:101], v[168:169], v[170:171]
	s_mov_b32 s2, 0x3a800000
	v_pk_fma_f32 v[100:101], v[100:101], s[2:3], v[196:197] op_sel_hi:[1,0,0]
	v_lshl_add_u64 v[108:109], v[108:109], 0, s[4:5]
	v_mul_f32_e32 v66, 0x4b800000, v101
	v_cmp_gt_f32_e32 vcc, s39, v101
	v_cvt_pk_bf16_f32 v104, v104, v105
	v_cvt_pk_bf16_f32 v105, v106, v107
	v_cvt_pk_bf16_f32 v106, v112, v113
	v_cvt_pk_bf16_f32 v107, v110, v111
	v_cmp_gt_f32_e64 s[42:43], s39, v100
	s_nop 0
	v_cndmask_b32_e32 v66, v101, v66, vcc
	v_rsq_f32_e32 v66, v66
	global_store_dwordx4 v[108:109], v[104:107], off sc1
	s_nop 1
	s_nop 0
	v_mul_f32_e32 v101, 0x45800000, v66
	v_cndmask_b32_e32 v102, v66, v101, vcc
	v_pk_fma_f32 v[98:99], v[98:99], v[102:103], v[146:147] op_sel_hi:[1,0,1]
	s_and_b64 vcc, exec, s[40:41]
	v_pk_fma_f32 v[96:97], v[96:97], v[102:103], v[144:145] op_sel_hi:[1,0,1]
	s_cbranch_vccnz .LBB0_576
	v_mov_b32_e32 v210, 0x3dd2d3e7
	v_pk_mul_f32 v[206:207], v[96:97], v[96:97]
	v_pk_mul_f32 v[208:209], v[98:99], v[98:99]
	v_pk_fma_f32 v[206:207], v[206:207], v[210:211], v[236:237] op_sel_hi:[1,0,0]
	v_pk_fma_f32 v[208:209], v[208:209], v[210:211], v[236:237] op_sel_hi:[1,0,0]
	v_pk_mul_f32 v[206:207], v[96:97], v[206:207]
	v_pk_mul_f32 v[208:209], v[98:99], v[208:209]
	v_exp_f32_e32 v206, v206
	v_exp_f32_e32 v207, v207
	v_exp_f32_e32 v208, v208
	v_exp_f32_e32 v209, v209
	v_pk_add_f32 v[206:207], v[206:207], 1.0 op_sel_hi:[1,0]
	v_pk_add_f32 v[208:209], v[208:209], 1.0 op_sel_hi:[1,0]
	v_rcp_f32_e32 v206, v206
	v_rcp_f32_e32 v207, v207
	v_rcp_f32_e32 v208, v208
	v_rcp_f32_e32 v209, v209
	v_pk_fma_f32 v[96:97], v[96:97], v[206:207], v[96:97] neg_lo:[1,0,0] neg_hi:[1,0,0]
	v_pk_fma_f32 v[98:99], v[98:99], v[208:209], v[98:99] neg_lo:[1,0,0] neg_hi:[1,0,0]
; __device__ __forceinline__ void store_bf16x8_wt(bf16* p, const f32x4 v0, const f32x4 v1) { u32x4 w; w.x = cvt_pk_bf16(v0[0], v0[1]); w.y = cvt_pk_bf16(v0[2], v0[3]); w.z = cvt_pk_bf16(v1[0], v1[1]); w.w = cvt_pk_bf16(v1[2], v1[3]); stg16_wt(p, w); }
; __device__ __forceinline__ float gelu_tanh(float x) {
;     const float C0 = 2.f * 0.7978845608028654f * L2E, C1 = 2.f * 0.7978845608028654f * 0.044715f * L2E;
;     const float e = __builtin_amdgcn_exp2f(x * __builtin_fmaf(x * x, C1, C0));
;     return __builtin_fmaf(-x, __builtin_amdgcn_rcpf(1.f + e), x);
; }
; template <bool FP8>
; __device__ __forceinline__ void epilogue(const Desc& d, const Acc& acc, const Tile& u, LAS unsigned char* lds) {
;     ...
;         for (int ai = 0; ai < 2; ++ai)
; #pragma unroll
;             for (int m = 0; m < 4; ++m)
; #pragma unroll
;                 for (int bj = 0; bj < 2; ++bj) { f32x4 v[2];
; #pragma unroll
;                     for (int n = 0; n < 2; ++n) { v[n] = acc[ai][bj][m][n] * rs[ai][m] + bv[bj][n];
;                         if (isg) { v[n][0] = gelu_tanh(v[n][0]); v[n][1] = gelu_tanh(v[n][1]); v[n][2] = gelu_tanh(v[n][2]); v[n][3] = gelu_tanh(v[n][3]); } }
;                     store_bf16x8_wt(O + (size_t)(row0 + ai * 128 + m * 16) * D + oc0 + bj * 128, v[0], v[1]); }
.LBB0_576:
	v_mov_b32_e32 v103, v102
	v_mov_b32_e32 v104, v102
	v_mov_b32_e32 v105, v102
	v_pk_fma_f32 v[94:95], v[94:95], v[104:105], v[142:143]
	s_and_b64 vcc, exec, s[40:41]
	v_pk_fma_f32 v[106:107], v[92:93], v[102:103], v[140:141]
	s_cbranch_vccnz .LBB0_578
	v_mov_b32_e32 v210, 0x3dd2d3e7
	v_pk_mul_f32 v[206:207], v[106:107], v[106:107]
	v_pk_mul_f32 v[208:209], v[94:95], v[94:95]
	v_pk_fma_f32 v[206:207], v[206:207], v[210:211], v[236:237] op_sel_hi:[1,0,0]
	v_pk_fma_f32 v[208:209], v[208:209], v[210:211], v[236:237] op_sel_hi:[1,0,0]
	v_pk_mul_f32 v[206:207], v[106:107], v[206:207]
	v_pk_mul_f32 v[208:209], v[94:95], v[208:209]
	v_exp_f32_e32 v206, v206
	v_exp_f32_e32 v207, v207
	v_exp_f32_e32 v208, v208
	v_exp_f32_e32 v209, v209
	v_pk_add_f32 v[206:207], v[206:207], 1.0 op_sel_hi:[1,0]
	v_pk_add_f32 v[208:209], v[208:209], 1.0 op_sel_hi:[1,0]
	v_rcp_f32_e32 v206, v206
	v_rcp_f32_e32 v207, v207
	v_rcp_f32_e32 v208, v208
	v_rcp_f32_e32 v209, v209
	v_pk_fma_f32 v[106:107], v[106:107], v[206:207], v[106:107] neg_lo:[1,0,0] neg_hi:[1,0,0]
	v_pk_fma_f32 v[94:95], v[94:95], v[208:209], v[94:95] neg_lo:[1,0,0] neg_hi:[1,0,0]
.LBB0_578:
	v_lshlrev_b64 v[92:93], 11, v[166:167]
	v_lshl_add_u64 v[92:93], v[124:125], 0, v[92:93]
	v_cvt_pk_bf16_f32 v96, v96, v97
	v_cvt_pk_bf16_f32 v97, v98, v99
	v_cvt_pk_bf16_f32 v98, v106, v107
	v_cvt_pk_bf16_f32 v99, v94, v95
	v_pk_fma_f32 v[90:91], v[90:91], v[104:105], v[138:139]
	global_store_dwordx4 v[92:93], v[96:99], off sc1
	s_nop 1
	s_and_b64 vcc, exec, s[40:41]
	v_pk_fma_f32 v[88:89], v[88:89], v[102:103], v[136:137]
	s_cbranch_vccnz .LBB0_580
	v_mov_b32_e32 v210, 0x3dd2d3e7
	v_pk_mul_f32 v[206:207], v[88:89], v[88:89]
	v_pk_mul_f32 v[208:209], v[90:91], v[90:91]
	v_pk_fma_f32 v[206:207], v[206:207], v[210:211], v[236:237] op_sel_hi:[1,0,0]
	v_pk_fma_f32 v[208:209], v[208:209], v[210:211], v[236:237] op_sel_hi:[1,0,0]
	v_pk_mul_f32 v[206:207], v[88:89], v[206:207]
	v_pk_mul_f32 v[208:209], v[90:91], v[208:209]
	v_exp_f32_e32 v206, v206
	v_exp_f32_e32 v207, v207
	v_exp_f32_e32 v208, v208
	v_exp_f32_e32 v209, v209
	v_pk_add_f32 v[206:207], v[206:207], 1.0 op_sel_hi:[1,0]
	v_pk_add_f32 v[208:209], v[208:209], 1.0 op_sel_hi:[1,0]
	v_rcp_f32_e32 v206, v206
	v_rcp_f32_e32 v207, v207
	v_rcp_f32_e32 v208, v208
	v_rcp_f32_e32 v209, v209
	v_pk_fma_f32 v[88:89], v[88:89], v[206:207], v[88:89] neg_lo:[1,0,0] neg_hi:[1,0,0]
	v_pk_fma_f32 v[90:91], v[90:91], v[208:209], v[90:91] neg_lo:[1,0,0] neg_hi:[1,0,0]
.LBB0_580:
	v_mov_b32_e32 v94, v102
	v_mov_b32_e32 v95, v102
	v_pk_fma_f32 v[86:87], v[86:87], v[94:95], v[134:135]
	s_and_b64 vcc, exec, s[40:41]
	v_pk_fma_f32 v[94:95], v[84:85], v[102:103], v[132:133]
	s_cbranch_vccnz .LBB0_582
	v_mov_b32_e32 v210, 0x3dd2d3e7
	v_pk_mul_f32 v[206:207], v[94:95], v[94:95]
	v_pk_mul_f32 v[208:209], v[86:87], v[86:87]
	v_pk_fma_f32 v[206:207], v[206:207], v[210:211], v[236:237] op_sel_hi:[1,0,0]
	v_pk_fma_f32 v[208:209], v[208:209], v[210:211], v[236:237] op_sel_hi:[1,0,0]
	v_pk_mul_f32 v[206:207], v[94:95], v[206:207]
	v_pk_mul_f32 v[208:209], v[86:87], v[208:209]
	v_exp_f32_e32 v206, v206
	v_exp_f32_e32 v207, v207
	v_exp_f32_e32 v208, v208
	v_exp_f32_e32 v209, v209
	v_pk_add_f32 v[206:207], v[206:207], 1.0 op_sel_hi:[1,0]
	v_pk_add_f32 v[208:209], v[208:209], 1.0 op_sel_hi:[1,0]
	v_rcp_f32_e32 v206, v206
	v_rcp_f32_e32 v207, v207
	v_rcp_f32_e32 v208, v208
	v_rcp_f32_e32 v209, v209
	v_pk_fma_f32 v[94:95], v[94:95], v[206:207], v[94:95] neg_lo:[1,0,0] neg_hi:[1,0,0]
	v_pk_fma_f32 v[86:87], v[86:87], v[208:209], v[86:87] neg_lo:[1,0,0] neg_hi:[1,0,0]
.LBB0_582:
	v_mul_f32_e32 v66, 0x4b800000, v100
	v_cndmask_b32_e64 v66, v100, v66, s[42:43]
	v_rsq_f32_e32 v66, v66
	v_lshl_add_u64 v[92:93], v[92:93], 0, s[4:5]
	v_cvt_pk_bf16_f32 v88, v88, v89
	v_cvt_pk_bf16_f32 v89, v90, v91
	v_mul_f32_e32 v84, 0x45800000, v66
	v_cvt_pk_bf16_f32 v90, v94, v95
	v_cvt_pk_bf16_f32 v91, v86, v87
	v_cndmask_b32_e64 v84, v66, v84, s[42:43]
	global_store_dwordx4 v[92:93], v[88:91], off sc1
	s_nop 1
	v_pk_fma_f32 v[82:83], v[82:83], v[84:85], v[146:147] op_sel_hi:[1,0,1]
	s_and_b64 vcc, exec, s[40:41]
	v_pk_fma_f32 v[80:81], v[80:81], v[84:85], v[144:145] op_sel_hi:[1,0,1]
	s_cbranch_vccnz .LBB0_584
	v_mov_b32_e32 v210, 0x3dd2d3e7
	v_pk_mul_f32 v[206:207], v[80:81], v[80:81]
	v_pk_mul_f32 v[208:209], v[82:83], v[82:83]
	v_pk_fma_f32 v[206:207], v[206:207], v[210:211], v[236:237] op_sel_hi:[1,0,0]
	v_pk_fma_f32 v[208:209], v[208:209], v[210:211], v[236:237] op_sel_hi:[1,0,0]
	v_pk_mul_f32 v[206:207], v[80:81], v[206:207]
	v_pk_mul_f32 v[208:209], v[82:83], v[208:209]
	v_exp_f32_e32 v206, v206
	v_exp_f32_e32 v207, v207
	v_exp_f32_e32 v208, v208
	v_exp_f32_e32 v209, v209
	v_pk_add_f32 v[206:207], v[206:207], 1.0 op_sel_hi:[1,0]
	v_pk_add_f32 v[208:209], v[208:209], 1.0 op_sel_hi:[1,0]
	v_rcp_f32_e32 v206, v206
	v_rcp_f32_e32 v207, v207
	v_rcp_f32_e32 v208, v208
	v_rcp_f32_e32 v209, v209
	v_pk_fma_f32 v[80:81], v[80:81], v[206:207], v[80:81] neg_lo:[1,0,0] neg_hi:[1,0,0]
	v_pk_fma_f32 v[82:83], v[82:83], v[208:209], v[82:83] neg_lo:[1,0,0] neg_hi:[1,0,0]
.LBB0_584:
	v_mov_b32_e32 v85, v84
	v_mov_b32_e32 v86, v84
	v_mov_b32_e32 v87, v84
	v_pk_fma_f32 v[78:79], v[78:79], v[86:87], v[142:143]
	s_and_b64 vcc, exec, s[40:41]
	v_pk_fma_f32 v[88:89], v[76:77], v[84:85], v[140:141]
	s_cbranch_vccnz .LBB0_586
	v_mov_b32_e32 v210, 0x3dd2d3e7
	v_pk_mul_f32 v[206:207], v[88:89], v[88:89]
	v_pk_mul_f32 v[208:209], v[78:79], v[78:79]
	v_pk_fma_f32 v[206:207], v[206:207], v[210:211], v[236:237] op_sel_hi:[1,0,0]
	v_pk_fma_f32 v[208:209], v[208:209], v[210:211], v[236:237] op_sel_hi:[1,0,0]
	v_pk_mul_f32 v[206:207], v[88:89], v[206:207]
	v_pk_mul_f32 v[208:209], v[78:79], v[208:209]
	v_exp_f32_e32 v206, v206
	v_exp_f32_e32 v207, v207
	v_exp_f32_e32 v208, v208
	v_exp_f32_e32 v209, v209
	v_pk_add_f32 v[206:207], v[206:207], 1.0 op_sel_hi:[1,0]
	v_pk_add_f32 v[208:209], v[208:209], 1.0 op_sel_hi:[1,0]
	v_rcp_f32_e32 v206, v206
	v_rcp_f32_e32 v207, v207
	v_rcp_f32_e32 v208, v208
	v_rcp_f32_e32 v209, v209
	v_pk_fma_f32 v[88:89], v[88:89], v[206:207], v[88:89] neg_lo:[1,0,0] neg_hi:[1,0,0]
	v_pk_fma_f32 v[78:79], v[78:79], v[208:209], v[78:79] neg_lo:[1,0,0] neg_hi:[1,0,0]
; __device__ __forceinline__ void store_bf16x8_wt(bf16* p, const f32x4 v0, const f32x4 v1) { u32x4 w; w.x = cvt_pk_bf16(v0[0], v0[1]); w.y = cvt_pk_bf16(v0[2], v0[3]); w.z = cvt_pk_bf16(v1[0], v1[1]); w.w = cvt_pk_bf16(v1[2], v1[3]); stg16_wt(p, w); }
; __device__ __forceinline__ float gelu_tanh(float x) {
;     const float C0 = 2.f * 0.7978845608028654f * L2E, C1 = 2.f * 0.7978845608028654f * 0.044715f * L2E;
;     const float e = __builtin_amdgcn_exp2f(x * __builtin_fmaf(x * x, C1, C0));
;     return __builtin_fmaf(-x, __builtin_amdgcn_rcpf(1.f + e), x);
; }
; template <bool FP8>
; __device__ __forceinline__ void epilogue(const Desc& d, const Acc& acc, const Tile& u, LAS unsigned char* lds) {
;     ...
;         for (int ai = 0; ai < 2; ++ai)
; #pragma unroll
;             for (int m = 0; m < 4; ++m)
; #pragma unroll
;                 for (int bj = 0; bj < 2; ++bj) { f32x4 v[2];
; #pragma unroll
;                     for (int n = 0; n < 2; ++n) { v[n] = acc[ai][bj][m][n] * rs[ai][m] + bv[bj][n];
;                         if (isg) { v[n][0] = gelu_tanh(v[n][0]); v[n][1] = gelu_tanh(v[n][1]); v[n][2] = gelu_tanh(v[n][2]); v[n][3] = gelu_tanh(v[n][3]); } }
;                     store_bf16x8_wt(O + (size_t)(row0 + ai * 128 + m * 16) * D + oc0 + bj * 128, v[0], v[1]); }
.LBB0_586:
	v_lshlrev_b64 v[76:77], 11, v[164:165]
	v_lshl_add_u64 v[76:77], v[124:125], 0, v[76:77]
	v_cvt_pk_bf16_f32 v80, v80, v81
	v_cvt_pk_bf16_f32 v81, v82, v83
	v_cvt_pk_bf16_f32 v82, v88, v89
	v_cvt_pk_bf16_f32 v83, v78, v79
	v_pk_fma_f32 v[74:75], v[74:75], v[86:87], v[138:139]
	global_store_dwordx4 v[76:77], v[80:83], off sc1
	s_nop 1
	s_and_b64 vcc, exec, s[40:41]
	v_pk_fma_f32 v[72:73], v[72:73], v[84:85], v[136:137]
	s_cbranch_vccnz .LBB0_588
	v_mov_b32_e32 v210, 0x3dd2d3e7
	v_pk_mul_f32 v[206:207], v[72:73], v[72:73]
	v_pk_mul_f32 v[208:209], v[74:75], v[74:75]
	v_pk_fma_f32 v[206:207], v[206:207], v[210:211], v[236:237] op_sel_hi:[1,0,0]
	v_pk_fma_f32 v[208:209], v[208:209], v[210:211], v[236:237] op_sel_hi:[1,0,0]
	v_pk_mul_f32 v[206:207], v[72:73], v[206:207]
	v_pk_mul_f32 v[208:209], v[74:75], v[208:209]
	v_exp_f32_e32 v206, v206
	v_exp_f32_e32 v207, v207
	v_exp_f32_e32 v208, v208
	v_exp_f32_e32 v209, v209
	v_pk_add_f32 v[206:207], v[206:207], 1.0 op_sel_hi:[1,0]
	v_pk_add_f32 v[208:209], v[208:209], 1.0 op_sel_hi:[1,0]
	v_rcp_f32_e32 v206, v206
	v_rcp_f32_e32 v207, v207
	v_rcp_f32_e32 v208, v208
	v_rcp_f32_e32 v209, v209
	v_pk_fma_f32 v[72:73], v[72:73], v[206:207], v[72:73] neg_lo:[1,0,0] neg_hi:[1,0,0]
	v_pk_fma_f32 v[74:75], v[74:75], v[208:209], v[74:75] neg_lo:[1,0,0] neg_hi:[1,0,0]
.LBB0_588:
	v_mov_b32_e32 v78, v84
	v_mov_b32_e32 v79, v84
	v_pk_fma_f32 v[78:79], v[70:71], v[78:79], v[134:135]
	s_and_b64 vcc, exec, s[40:41]
	v_pk_fma_f32 v[80:81], v[68:69], v[84:85], v[132:133]
	s_cbranch_vccnz .LBB0_590
	v_mov_b32_e32 v210, 0x3dd2d3e7
	v_pk_mul_f32 v[206:207], v[80:81], v[80:81]
	v_pk_mul_f32 v[208:209], v[78:79], v[78:79]
	v_pk_fma_f32 v[206:207], v[206:207], v[210:211], v[236:237] op_sel_hi:[1,0,0]
	v_pk_fma_f32 v[208:209], v[208:209], v[210:211], v[236:237] op_sel_hi:[1,0,0]
	v_pk_mul_f32 v[206:207], v[80:81], v[206:207]
	v_pk_mul_f32 v[208:209], v[78:79], v[208:209]
	v_exp_f32_e32 v206, v206
	v_exp_f32_e32 v207, v207
	v_exp_f32_e32 v208, v208
	v_exp_f32_e32 v209, v209
	v_pk_add_f32 v[206:207], v[206:207], 1.0 op_sel_hi:[1,0]
	v_pk_add_f32 v[208:209], v[208:209], 1.0 op_sel_hi:[1,0]
	v_rcp_f32_e32 v206, v206
	v_rcp_f32_e32 v207, v207
	v_rcp_f32_e32 v208, v208
	v_rcp_f32_e32 v209, v209
	v_pk_fma_f32 v[80:81], v[80:81], v[206:207], v[80:81] neg_lo:[1,0,0] neg_hi:[1,0,0]
	v_pk_fma_f32 v[78:79], v[78:79], v[208:209], v[78:79] neg_lo:[1,0,0] neg_hi:[1,0,0]
.LBB0_590:
	s_waitcnt lgkmcnt(2)
	v_pk_add_f32 v[68:69], v[160:161], v[162:163]
	v_lshl_add_u64 v[76:77], v[76:77], 0, s[4:5]
	v_pk_fma_f32 v[68:69], v[68:69], s[2:3], v[196:197] op_sel_hi:[1,0,0]
	v_cvt_pk_bf16_f32 v72, v72, v73
	v_cvt_pk_bf16_f32 v73, v74, v75
	v_cvt_pk_bf16_f32 v74, v80, v81
	v_cvt_pk_bf16_f32 v75, v78, v79
	s_nop 0
	v_mul_f32_e32 v66, 0x4b800000, v69
	v_cmp_gt_f32_e32 vcc, s39, v69
	global_store_dwordx4 v[76:77], v[72:75], off sc1
	s_nop 1
	v_cmp_gt_f32_e64 s[42:43], s39, v68
	s_nop 0
	v_cndmask_b32_e32 v66, v69, v66, vcc
	v_rsq_f32_e32 v66, v66
	s_nop 0
	v_mul_f32_e32 v69, 0x45800000, v66
	v_cndmask_b32_e32 v70, v66, v69, vcc
	v_pk_fma_f32 v[64:65], v[64:65], v[70:71], v[146:147] op_sel_hi:[1,0,1]
	s_and_b64 vcc, exec, s[40:41]
	v_pk_fma_f32 v[62:63], v[62:63], v[70:71], v[144:145] op_sel_hi:[1,0,1]
	s_cbranch_vccnz .LBB0_592
	v_mov_b32_e32 v210, 0x3dd2d3e7
	v_pk_mul_f32 v[206:207], v[62:63], v[62:63]
	v_pk_mul_f32 v[208:209], v[64:65], v[64:65]
	v_pk_fma_f32 v[206:207], v[206:207], v[210:211], v[236:237] op_sel_hi:[1,0,0]
	v_pk_fma_f32 v[208:209], v[208:209], v[210:211], v[236:237] op_sel_hi:[1,0,0]
	v_pk_mul_f32 v[206:207], v[62:63], v[206:207]
	v_pk_mul_f32 v[208:209], v[64:65], v[208:209]
	v_exp_f32_e32 v206, v206
	v_exp_f32_e32 v207, v207
	v_exp_f32_e32 v208, v208
	v_exp_f32_e32 v209, v209
	v_pk_add_f32 v[206:207], v[206:207], 1.0 op_sel_hi:[1,0]
	v_pk_add_f32 v[208:209], v[208:209], 1.0 op_sel_hi:[1,0]
	v_rcp_f32_e32 v206, v206
	v_rcp_f32_e32 v207, v207
	v_rcp_f32_e32 v208, v208
	v_rcp_f32_e32 v209, v209
	v_pk_fma_f32 v[62:63], v[62:63], v[206:207], v[62:63] neg_lo:[1,0,0] neg_hi:[1,0,0]
	v_pk_fma_f32 v[64:65], v[64:65], v[208:209], v[64:65] neg_lo:[1,0,0] neg_hi:[1,0,0]
.LBB0_592:
	v_mov_b32_e32 v71, v70
	v_mov_b32_e32 v72, v70
	v_mov_b32_e32 v73, v70
	v_pk_fma_f32 v[60:61], v[60:61], v[72:73], v[142:143]
	s_and_b64 vcc, exec, s[40:41]
	v_pk_fma_f32 v[74:75], v[58:59], v[70:71], v[140:141]
	s_cbranch_vccnz .LBB0_594
	v_mov_b32_e32 v210, 0x3dd2d3e7
	v_pk_mul_f32 v[206:207], v[74:75], v[74:75]
	v_pk_mul_f32 v[208:209], v[60:61], v[60:61]
	v_pk_fma_f32 v[206:207], v[206:207], v[210:211], v[236:237] op_sel_hi:[1,0,0]
	v_pk_fma_f32 v[208:209], v[208:209], v[210:211], v[236:237] op_sel_hi:[1,0,0]
	v_pk_mul_f32 v[206:207], v[74:75], v[206:207]
	v_pk_mul_f32 v[208:209], v[60:61], v[208:209]
	v_exp_f32_e32 v206, v206
	v_exp_f32_e32 v207, v207
	v_exp_f32_e32 v208, v208
	v_exp_f32_e32 v209, v209
	v_pk_add_f32 v[206:207], v[206:207], 1.0 op_sel_hi:[1,0]
	v_pk_add_f32 v[208:209], v[208:209], 1.0 op_sel_hi:[1,0]
	v_rcp_f32_e32 v206, v206
	v_rcp_f32_e32 v207, v207
	v_rcp_f32_e32 v208, v208
	v_rcp_f32_e32 v209, v209
	v_pk_fma_f32 v[74:75], v[74:75], v[206:207], v[74:75] neg_lo:[1,0,0] neg_hi:[1,0,0]
	v_pk_fma_f32 v[60:61], v[60:61], v[208:209], v[60:61] neg_lo:[1,0,0] neg_hi:[1,0,0]
; __device__ __forceinline__ void store_bf16x8_wt(bf16* p, const f32x4 v0, const f32x4 v1) { u32x4 w; w.x = cvt_pk_bf16(v0[0], v0[1]); w.y = cvt_pk_bf16(v0[2], v0[3]); w.z = cvt_pk_bf16(v1[0], v1[1]); w.w = cvt_pk_bf16(v1[2], v1[3]); stg16_wt(p, w); }
; __device__ __forceinline__ float gelu_tanh(float x) {
;     const float C0 = 2.f * 0.7978845608028654f * L2E, C1 = 2.f * 0.7978845608028654f * 0.044715f * L2E;
;     const float e = __builtin_amdgcn_exp2f(x * __builtin_fmaf(x * x, C1, C0));
;     return __builtin_fmaf(-x, __builtin_amdgcn_rcpf(1.f + e), x);
; }
; template <bool FP8>
; __device__ __forceinline__ void epilogue(const Desc& d, const Acc& acc, const Tile& u, LAS unsigned char* lds) {
;     ...
;         for (int ai = 0; ai < 2; ++ai)
; #pragma unroll
;             for (int m = 0; m < 4; ++m)
; #pragma unroll
;                 for (int bj = 0; bj < 2; ++bj) { f32x4 v[2];
; #pragma unroll
;                     for (int n = 0; n < 2; ++n) { v[n] = acc[ai][bj][m][n] * rs[ai][m] + bv[bj][n];
;                         if (isg) { v[n][0] = gelu_tanh(v[n][0]); v[n][1] = gelu_tanh(v[n][1]); v[n][2] = gelu_tanh(v[n][2]); v[n][3] = gelu_tanh(v[n][3]); } }
;                     store_bf16x8_wt(O + (size_t)(row0 + ai * 128 + m * 16) * D + oc0 + bj * 128, v[0], v[1]); }
.LBB0_594:
	v_lshlrev_b64 v[58:59], 11, v[158:159]
	v_lshl_add_u64 v[58:59], v[124:125], 0, v[58:59]
	v_cvt_pk_bf16_f32 v62, v62, v63
	v_cvt_pk_bf16_f32 v63, v64, v65
	v_cvt_pk_bf16_f32 v64, v74, v75
	v_cvt_pk_bf16_f32 v65, v60, v61
	v_pk_fma_f32 v[56:57], v[56:57], v[72:73], v[138:139]
	global_store_dwordx4 v[58:59], v[62:65], off sc1
	s_nop 1
	s_and_b64 vcc, exec, s[40:41]
	v_pk_fma_f32 v[54:55], v[54:55], v[70:71], v[136:137]
	s_cbranch_vccnz .LBB0_596
	v_mov_b32_e32 v210, 0x3dd2d3e7
	v_pk_mul_f32 v[206:207], v[54:55], v[54:55]
	v_pk_mul_f32 v[208:209], v[56:57], v[56:57]
	v_pk_fma_f32 v[206:207], v[206:207], v[210:211], v[236:237] op_sel_hi:[1,0,0]
	v_pk_fma_f32 v[208:209], v[208:209], v[210:211], v[236:237] op_sel_hi:[1,0,0]
	v_pk_mul_f32 v[206:207], v[54:55], v[206:207]
	v_pk_mul_f32 v[208:209], v[56:57], v[208:209]
	v_exp_f32_e32 v206, v206
	v_exp_f32_e32 v207, v207
	v_exp_f32_e32 v208, v208
	v_exp_f32_e32 v209, v209
	v_pk_add_f32 v[206:207], v[206:207], 1.0 op_sel_hi:[1,0]
	v_pk_add_f32 v[208:209], v[208:209], 1.0 op_sel_hi:[1,0]
	v_rcp_f32_e32 v206, v206
	v_rcp_f32_e32 v207, v207
	v_rcp_f32_e32 v208, v208
	v_rcp_f32_e32 v209, v209
	v_pk_fma_f32 v[54:55], v[54:55], v[206:207], v[54:55] neg_lo:[1,0,0] neg_hi:[1,0,0]
	v_pk_fma_f32 v[56:57], v[56:57], v[208:209], v[56:57] neg_lo:[1,0,0] neg_hi:[1,0,0]
.LBB0_596:
	v_mov_b32_e32 v60, v70
	v_mov_b32_e32 v61, v70
	v_pk_fma_f32 v[52:53], v[52:53], v[60:61], v[134:135]
	s_and_b64 vcc, exec, s[40:41]
	v_pk_fma_f32 v[60:61], v[50:51], v[70:71], v[132:133]
	s_cbranch_vccnz .LBB0_598
	v_mov_b32_e32 v210, 0x3dd2d3e7
	v_pk_mul_f32 v[206:207], v[60:61], v[60:61]
	v_pk_mul_f32 v[208:209], v[52:53], v[52:53]
	v_pk_fma_f32 v[206:207], v[206:207], v[210:211], v[236:237] op_sel_hi:[1,0,0]
	v_pk_fma_f32 v[208:209], v[208:209], v[210:211], v[236:237] op_sel_hi:[1,0,0]
	v_pk_mul_f32 v[206:207], v[60:61], v[206:207]
	v_pk_mul_f32 v[208:209], v[52:53], v[208:209]
	v_exp_f32_e32 v206, v206
	v_exp_f32_e32 v207, v207
	v_exp_f32_e32 v208, v208
	v_exp_f32_e32 v209, v209
	v_pk_add_f32 v[206:207], v[206:207], 1.0 op_sel_hi:[1,0]
	v_pk_add_f32 v[208:209], v[208:209], 1.0 op_sel_hi:[1,0]
	v_rcp_f32_e32 v206, v206
	v_rcp_f32_e32 v207, v207
	v_rcp_f32_e32 v208, v208
	v_rcp_f32_e32 v209, v209
	v_pk_fma_f32 v[60:61], v[60:61], v[206:207], v[60:61] neg_lo:[1,0,0] neg_hi:[1,0,0]
	v_pk_fma_f32 v[52:53], v[52:53], v[208:209], v[52:53] neg_lo:[1,0,0] neg_hi:[1,0,0]
.LBB0_598:
	v_mul_f32_e32 v50, 0x4b800000, v68
	v_cndmask_b32_e64 v50, v68, v50, s[42:43]
	v_rsq_f32_e32 v50, v50
	v_lshl_add_u64 v[58:59], v[58:59], 0, s[4:5]
	v_cvt_pk_bf16_f32 v54, v54, v55
	v_cvt_pk_bf16_f32 v55, v56, v57
	v_mul_f32_e32 v51, 0x45800000, v50
	v_cvt_pk_bf16_f32 v56, v60, v61
	v_cvt_pk_bf16_f32 v57, v52, v53
	v_cndmask_b32_e64 v50, v50, v51, s[42:43]
	global_store_dwordx4 v[58:59], v[54:57], off sc1
	s_nop 1
	v_pk_fma_f32 v[48:49], v[48:49], v[50:51], v[146:147] op_sel_hi:[1,0,1]
	s_and_b64 vcc, exec, s[40:41]
	v_pk_fma_f32 v[46:47], v[46:47], v[50:51], v[144:145] op_sel_hi:[1,0,1]
	s_cbranch_vccnz .LBB0_600
	v_mov_b32_e32 v210, 0x3dd2d3e7
	v_pk_mul_f32 v[206:207], v[46:47], v[46:47]
	v_pk_mul_f32 v[208:209], v[48:49], v[48:49]
	v_pk_fma_f32 v[206:207], v[206:207], v[210:211], v[236:237] op_sel_hi:[1,0,0]
	v_pk_fma_f32 v[208:209], v[208:209], v[210:211], v[236:237] op_sel_hi:[1,0,0]
	v_pk_mul_f32 v[206:207], v[46:47], v[206:207]
	v_pk_mul_f32 v[208:209], v[48:49], v[208:209]
	v_exp_f32_e32 v206, v206
	v_exp_f32_e32 v207, v207
	v_exp_f32_e32 v208, v208
	v_exp_f32_e32 v209, v209
	v_pk_add_f32 v[206:207], v[206:207], 1.0 op_sel_hi:[1,0]
	v_pk_add_f32 v[208:209], v[208:209], 1.0 op_sel_hi:[1,0]
	v_rcp_f32_e32 v206, v206
	v_rcp_f32_e32 v207, v207
	v_rcp_f32_e32 v208, v208
	v_rcp_f32_e32 v209, v209
	v_pk_fma_f32 v[46:47], v[46:47], v[206:207], v[46:47] neg_lo:[1,0,0] neg_hi:[1,0,0]
	v_pk_fma_f32 v[48:49], v[48:49], v[208:209], v[48:49] neg_lo:[1,0,0] neg_hi:[1,0,0]
.LBB0_600:
	v_mov_b32_e32 v51, v50
	v_mov_b32_e32 v52, v50
	v_mov_b32_e32 v53, v50
	v_pk_fma_f32 v[44:45], v[44:45], v[52:53], v[142:143]
	s_and_b64 vcc, exec, s[40:41]
	v_pk_fma_f32 v[54:55], v[42:43], v[50:51], v[140:141]
	s_cbranch_vccnz .LBB0_602
	v_mov_b32_e32 v210, 0x3dd2d3e7
	v_pk_mul_f32 v[206:207], v[54:55], v[54:55]
	v_pk_mul_f32 v[208:209], v[44:45], v[44:45]
	v_pk_fma_f32 v[206:207], v[206:207], v[210:211], v[236:237] op_sel_hi:[1,0,0]
	v_pk_fma_f32 v[208:209], v[208:209], v[210:211], v[236:237] op_sel_hi:[1,0,0]
	v_pk_mul_f32 v[206:207], v[54:55], v[206:207]
	v_pk_mul_f32 v[208:209], v[44:45], v[208:209]
	v_exp_f32_e32 v206, v206
	v_exp_f32_e32 v207, v207
	v_exp_f32_e32 v208, v208
	v_exp_f32_e32 v209, v209
	v_pk_add_f32 v[206:207], v[206:207], 1.0 op_sel_hi:[1,0]
	v_pk_add_f32 v[208:209], v[208:209], 1.0 op_sel_hi:[1,0]
	v_rcp_f32_e32 v206, v206
	v_rcp_f32_e32 v207, v207
	v_rcp_f32_e32 v208, v208
	v_rcp_f32_e32 v209, v209
	v_pk_fma_f32 v[54:55], v[54:55], v[206:207], v[54:55] neg_lo:[1,0,0] neg_hi:[1,0,0]
	v_pk_fma_f32 v[44:45], v[44:45], v[208:209], v[44:45] neg_lo:[1,0,0] neg_hi:[1,0,0]
; __device__ __forceinline__ void store_bf16x8_wt(bf16* p, const f32x4 v0, const f32x4 v1) { u32x4 w; w.x = cvt_pk_bf16(v0[0], v0[1]); w.y = cvt_pk_bf16(v0[2], v0[3]); w.z = cvt_pk_bf16(v1[0], v1[1]); w.w = cvt_pk_bf16(v1[2], v1[3]); stg16_wt(p, w); }
; __device__ __forceinline__ float gelu_tanh(float x) {
;     const float C0 = 2.f * 0.7978845608028654f * L2E, C1 = 2.f * 0.7978845608028654f * 0.044715f * L2E;
;     const float e = __builtin_amdgcn_exp2f(x * __builtin_fmaf(x * x, C1, C0));
;     return __builtin_fmaf(-x, __builtin_amdgcn_rcpf(1.f + e), x);
; }
; template <bool FP8>
; __device__ __forceinline__ void epilogue(const Desc& d, const Acc& acc, const Tile& u, LAS unsigned char* lds) {
;     ...
;         for (int ai = 0; ai < 2; ++ai)
; #pragma unroll
;             for (int m = 0; m < 4; ++m)
; #pragma unroll
;                 for (int bj = 0; bj < 2; ++bj) { f32x4 v[2];
; #pragma unroll
;                     for (int n = 0; n < 2; ++n) { v[n] = acc[ai][bj][m][n] * rs[ai][m] + bv[bj][n];
;                         if (isg) { v[n][0] = gelu_tanh(v[n][0]); v[n][1] = gelu_tanh(v[n][1]); v[n][2] = gelu_tanh(v[n][2]); v[n][3] = gelu_tanh(v[n][3]); } }
;                     store_bf16x8_wt(O + (size_t)(row0 + ai * 128 + m * 16) * D + oc0 + bj * 128, v[0], v[1]); }
.LBB0_602:
	v_lshlrev_b64 v[42:43], 11, v[156:157]
	v_lshl_add_u64 v[42:43], v[124:125], 0, v[42:43]
	v_cvt_pk_bf16_f32 v46, v46, v47
	v_cvt_pk_bf16_f32 v47, v48, v49
	v_cvt_pk_bf16_f32 v48, v54, v55
	v_cvt_pk_bf16_f32 v49, v44, v45
	v_pk_fma_f32 v[40:41], v[40:41], v[52:53], v[138:139]
	global_store_dwordx4 v[42:43], v[46:49], off sc1
	s_nop 1
	s_and_b64 vcc, exec, s[40:41]
	v_pk_fma_f32 v[38:39], v[38:39], v[50:51], v[136:137]
	s_cbranch_vccnz .LBB0_604
	v_mov_b32_e32 v210, 0x3dd2d3e7
	v_pk_mul_f32 v[206:207], v[38:39], v[38:39]
	v_pk_mul_f32 v[208:209], v[40:41], v[40:41]
	v_pk_fma_f32 v[206:207], v[206:207], v[210:211], v[236:237] op_sel_hi:[1,0,0]
	v_pk_fma_f32 v[208:209], v[208:209], v[210:211], v[236:237] op_sel_hi:[1,0,0]
	v_pk_mul_f32 v[206:207], v[38:39], v[206:207]
	v_pk_mul_f32 v[208:209], v[40:41], v[208:209]
	v_exp_f32_e32 v206, v206
	v_exp_f32_e32 v207, v207
	v_exp_f32_e32 v208, v208
	v_exp_f32_e32 v209, v209
	v_pk_add_f32 v[206:207], v[206:207], 1.0 op_sel_hi:[1,0]
	v_pk_add_f32 v[208:209], v[208:209], 1.0 op_sel_hi:[1,0]
	v_rcp_f32_e32 v206, v206
	v_rcp_f32_e32 v207, v207
	v_rcp_f32_e32 v208, v208
	v_rcp_f32_e32 v209, v209
	v_pk_fma_f32 v[38:39], v[38:39], v[206:207], v[38:39] neg_lo:[1,0,0] neg_hi:[1,0,0]
	v_pk_fma_f32 v[40:41], v[40:41], v[208:209], v[40:41] neg_lo:[1,0,0] neg_hi:[1,0,0]
.LBB0_604:
	v_mov_b32_e32 v44, v50
	v_mov_b32_e32 v45, v50
	v_pk_fma_f32 v[44:45], v[36:37], v[44:45], v[134:135]
	s_and_b64 vcc, exec, s[40:41]
	v_pk_fma_f32 v[46:47], v[34:35], v[50:51], v[132:133]
	s_cbranch_vccnz .LBB0_606
	v_mov_b32_e32 v210, 0x3dd2d3e7
	v_pk_mul_f32 v[206:207], v[46:47], v[46:47]
	v_pk_mul_f32 v[208:209], v[44:45], v[44:45]
	v_pk_fma_f32 v[206:207], v[206:207], v[210:211], v[236:237] op_sel_hi:[1,0,0]
	v_pk_fma_f32 v[208:209], v[208:209], v[210:211], v[236:237] op_sel_hi:[1,0,0]
	v_pk_mul_f32 v[206:207], v[46:47], v[206:207]
	v_pk_mul_f32 v[208:209], v[44:45], v[208:209]
	v_exp_f32_e32 v206, v206
	v_exp_f32_e32 v207, v207
	v_exp_f32_e32 v208, v208
	v_exp_f32_e32 v209, v209
	v_pk_add_f32 v[206:207], v[206:207], 1.0 op_sel_hi:[1,0]
	v_pk_add_f32 v[208:209], v[208:209], 1.0 op_sel_hi:[1,0]
	v_rcp_f32_e32 v206, v206
	v_rcp_f32_e32 v207, v207
	v_rcp_f32_e32 v208, v208
	v_rcp_f32_e32 v209, v209
	v_pk_fma_f32 v[46:47], v[46:47], v[206:207], v[46:47] neg_lo:[1,0,0] neg_hi:[1,0,0]
	v_pk_fma_f32 v[44:45], v[44:45], v[208:209], v[44:45] neg_lo:[1,0,0] neg_hi:[1,0,0]
.LBB0_606:
	s_waitcnt lgkmcnt(0)
	v_pk_add_f32 v[34:35], v[152:153], v[154:155]
	v_lshl_add_u64 v[42:43], v[42:43], 0, s[4:5]
	v_pk_fma_f32 v[34:35], v[34:35], s[2:3], v[196:197] op_sel_hi:[1,0,0]
	v_cvt_pk_bf16_f32 v38, v38, v39
	v_cvt_pk_bf16_f32 v39, v40, v41
	v_cvt_pk_bf16_f32 v40, v46, v47
	v_cvt_pk_bf16_f32 v41, v44, v45
	s_nop 0
	v_mul_f32_e32 v36, 0x4b800000, v35
	v_cmp_gt_f32_e32 vcc, s39, v35
	global_store_dwordx4 v[42:43], v[38:41], off sc1
	s_nop 1
	v_cmp_gt_f32_e64 s[42:43], s39, v34
	s_nop 0
	v_cndmask_b32_e32 v35, v35, v36, vcc
	v_rsq_f32_e32 v35, v35
	s_nop 0
	v_mul_f32_e32 v36, 0x45800000, v35
	v_cndmask_b32_e32 v36, v35, v36, vcc
	v_pk_fma_f32 v[32:33], v[32:33], v[36:37], v[146:147] op_sel_hi:[1,0,1]
	s_and_b64 vcc, exec, s[40:41]
	v_pk_fma_f32 v[30:31], v[30:31], v[36:37], v[144:145] op_sel_hi:[1,0,1]
	s_cbranch_vccnz .LBB0_608
	v_mov_b32_e32 v210, 0x3dd2d3e7
	v_pk_mul_f32 v[206:207], v[30:31], v[30:31]
	v_pk_mul_f32 v[208:209], v[32:33], v[32:33]
	v_pk_fma_f32 v[206:207], v[206:207], v[210:211], v[236:237] op_sel_hi:[1,0,0]
	v_pk_fma_f32 v[208:209], v[208:209], v[210:211], v[236:237] op_sel_hi:[1,0,0]
	v_pk_mul_f32 v[206:207], v[30:31], v[206:207]
	v_pk_mul_f32 v[208:209], v[32:33], v[208:209]
	v_exp_f32_e32 v206, v206
	v_exp_f32_e32 v207, v207
	v_exp_f32_e32 v208, v208
	v_exp_f32_e32 v209, v209
	v_pk_add_f32 v[206:207], v[206:207], 1.0 op_sel_hi:[1,0]
	v_pk_add_f32 v[208:209], v[208:209], 1.0 op_sel_hi:[1,0]
	v_rcp_f32_e32 v206, v206
	v_rcp_f32_e32 v207, v207
	v_rcp_f32_e32 v208, v208
	v_rcp_f32_e32 v209, v209
	v_pk_fma_f32 v[30:31], v[30:31], v[206:207], v[30:31] neg_lo:[1,0,0] neg_hi:[1,0,0]
	v_pk_fma_f32 v[32:33], v[32:33], v[208:209], v[32:33] neg_lo:[1,0,0] neg_hi:[1,0,0]
.LBB0_608:
	v_mov_b32_e32 v37, v36
	v_mov_b32_e32 v38, v36
	v_mov_b32_e32 v39, v36
	v_pk_fma_f32 v[28:29], v[28:29], v[38:39], v[142:143]
	s_and_b64 vcc, exec, s[40:41]
	v_pk_fma_f32 v[40:41], v[26:27], v[36:37], v[140:141]
	s_cbranch_vccnz .LBB0_610
	v_mov_b32_e32 v210, 0x3dd2d3e7
	v_pk_mul_f32 v[206:207], v[40:41], v[40:41]
	v_pk_mul_f32 v[208:209], v[28:29], v[28:29]
	v_pk_fma_f32 v[206:207], v[206:207], v[210:211], v[236:237] op_sel_hi:[1,0,0]
	v_pk_fma_f32 v[208:209], v[208:209], v[210:211], v[236:237] op_sel_hi:[1,0,0]
	v_pk_mul_f32 v[206:207], v[40:41], v[206:207]
	v_pk_mul_f32 v[208:209], v[28:29], v[208:209]
	v_exp_f32_e32 v206, v206
	v_exp_f32_e32 v207, v207
	v_exp_f32_e32 v208, v208
	v_exp_f32_e32 v209, v209
	v_pk_add_f32 v[206:207], v[206:207], 1.0 op_sel_hi:[1,0]
	v_pk_add_f32 v[208:209], v[208:209], 1.0 op_sel_hi:[1,0]
	v_rcp_f32_e32 v206, v206
	v_rcp_f32_e32 v207, v207
	v_rcp_f32_e32 v208, v208
	v_rcp_f32_e32 v209, v209
	v_pk_fma_f32 v[40:41], v[40:41], v[206:207], v[40:41] neg_lo:[1,0,0] neg_hi:[1,0,0]
	v_pk_fma_f32 v[28:29], v[28:29], v[208:209], v[28:29] neg_lo:[1,0,0] neg_hi:[1,0,0]
; __device__ __forceinline__ void store_bf16x8_wt(bf16* p, const f32x4 v0, const f32x4 v1) { u32x4 w; w.x = cvt_pk_bf16(v0[0], v0[1]); w.y = cvt_pk_bf16(v0[2], v0[3]); w.z = cvt_pk_bf16(v1[0], v1[1]); w.w = cvt_pk_bf16(v1[2], v1[3]); stg16_wt(p, w); }
; __device__ __forceinline__ float gelu_tanh(float x) {
;     const float C0 = 2.f * 0.7978845608028654f * L2E, C1 = 2.f * 0.7978845608028654f * 0.044715f * L2E;
;     const float e = __builtin_amdgcn_exp2f(x * __builtin_fmaf(x * x, C1, C0));
;     return __builtin_fmaf(-x, __builtin_amdgcn_rcpf(1.f + e), x);
; }
; template <bool FP8>
; __device__ __forceinline__ void epilogue(const Desc& d, const Acc& acc, const Tile& u, LAS unsigned char* lds) {
;     ...
;         for (int ai = 0; ai < 2; ++ai)
; #pragma unroll
;             for (int m = 0; m < 4; ++m)
; #pragma unroll
;                 for (int bj = 0; bj < 2; ++bj) { f32x4 v[2];
; #pragma unroll
;                     for (int n = 0; n < 2; ++n) { v[n] = acc[ai][bj][m][n] * rs[ai][m] + bv[bj][n];
;                         if (isg) { v[n][0] = gelu_tanh(v[n][0]); v[n][1] = gelu_tanh(v[n][1]); v[n][2] = gelu_tanh(v[n][2]); v[n][3] = gelu_tanh(v[n][3]); } }
;                     store_bf16x8_wt(O + (size_t)(row0 + ai * 128 + m * 16) * D + oc0 + bj * 128, v[0], v[1]); }
.LBB0_610:
	v_lshlrev_b64 v[26:27], 11, v[150:151]
	v_lshl_add_u64 v[26:27], v[124:125], 0, v[26:27]
	v_cvt_pk_bf16_f32 v30, v30, v31
	v_cvt_pk_bf16_f32 v31, v32, v33
	v_cvt_pk_bf16_f32 v32, v40, v41
	v_cvt_pk_bf16_f32 v33, v28, v29
	v_pk_fma_f32 v[24:25], v[24:25], v[38:39], v[138:139]
	global_store_dwordx4 v[26:27], v[30:33], off sc1
	s_nop 1
	s_and_b64 vcc, exec, s[40:41]
	v_pk_fma_f32 v[22:23], v[22:23], v[36:37], v[136:137]
	s_cbranch_vccnz .LBB0_612
	v_mov_b32_e32 v210, 0x3dd2d3e7
	v_pk_mul_f32 v[206:207], v[22:23], v[22:23]
	v_pk_mul_f32 v[208:209], v[24:25], v[24:25]
	v_pk_fma_f32 v[206:207], v[206:207], v[210:211], v[236:237] op_sel_hi:[1,0,0]
	v_pk_fma_f32 v[208:209], v[208:209], v[210:211], v[236:237] op_sel_hi:[1,0,0]
	v_pk_mul_f32 v[206:207], v[22:23], v[206:207]
	v_pk_mul_f32 v[208:209], v[24:25], v[208:209]
	v_exp_f32_e32 v206, v206
	v_exp_f32_e32 v207, v207
	v_exp_f32_e32 v208, v208
	v_exp_f32_e32 v209, v209
	v_pk_add_f32 v[206:207], v[206:207], 1.0 op_sel_hi:[1,0]
	v_pk_add_f32 v[208:209], v[208:209], 1.0 op_sel_hi:[1,0]
	v_rcp_f32_e32 v206, v206
	v_rcp_f32_e32 v207, v207
	v_rcp_f32_e32 v208, v208
	v_rcp_f32_e32 v209, v209
	v_pk_fma_f32 v[22:23], v[22:23], v[206:207], v[22:23] neg_lo:[1,0,0] neg_hi:[1,0,0]
	v_pk_fma_f32 v[24:25], v[24:25], v[208:209], v[24:25] neg_lo:[1,0,0] neg_hi:[1,0,0]
.LBB0_612:
	v_mov_b32_e32 v28, v36
	v_mov_b32_e32 v29, v36
	v_pk_fma_f32 v[20:21], v[20:21], v[28:29], v[134:135]
	s_and_b64 vcc, exec, s[40:41]
	v_pk_fma_f32 v[28:29], v[18:19], v[36:37], v[132:133]
	s_cbranch_vccnz .LBB0_614
	v_mov_b32_e32 v210, 0x3dd2d3e7
	v_pk_mul_f32 v[206:207], v[28:29], v[28:29]
	v_pk_mul_f32 v[208:209], v[20:21], v[20:21]
	v_pk_fma_f32 v[206:207], v[206:207], v[210:211], v[236:237] op_sel_hi:[1,0,0]
	v_pk_fma_f32 v[208:209], v[208:209], v[210:211], v[236:237] op_sel_hi:[1,0,0]
	v_pk_mul_f32 v[206:207], v[28:29], v[206:207]
	v_pk_mul_f32 v[208:209], v[20:21], v[208:209]
	v_exp_f32_e32 v206, v206
	v_exp_f32_e32 v207, v207
	v_exp_f32_e32 v208, v208
	v_exp_f32_e32 v209, v209
	v_pk_add_f32 v[206:207], v[206:207], 1.0 op_sel_hi:[1,0]
	v_pk_add_f32 v[208:209], v[208:209], 1.0 op_sel_hi:[1,0]
	v_rcp_f32_e32 v206, v206
	v_rcp_f32_e32 v207, v207
	v_rcp_f32_e32 v208, v208
	v_rcp_f32_e32 v209, v209
	v_pk_fma_f32 v[28:29], v[28:29], v[206:207], v[28:29] neg_lo:[1,0,0] neg_hi:[1,0,0]
	v_pk_fma_f32 v[20:21], v[20:21], v[208:209], v[20:21] neg_lo:[1,0,0] neg_hi:[1,0,0]
.LBB0_614:
	v_mul_f32_e32 v18, 0x4b800000, v34
	v_cndmask_b32_e64 v18, v34, v18, s[42:43]
	v_rsq_f32_e32 v18, v18
	v_lshl_add_u64 v[26:27], v[26:27], 0, s[4:5]
	v_cvt_pk_bf16_f32 v22, v22, v23
	v_cvt_pk_bf16_f32 v23, v24, v25
	v_mul_f32_e32 v19, 0x45800000, v18
	v_cvt_pk_bf16_f32 v24, v28, v29
	v_cvt_pk_bf16_f32 v25, v20, v21
	v_cndmask_b32_e64 v18, v18, v19, s[42:43]
	global_store_dwordx4 v[26:27], v[22:25], off sc1
	s_nop 1
	v_pk_fma_f32 v[16:17], v[16:17], v[18:19], v[146:147] op_sel_hi:[1,0,1]
	s_and_b64 vcc, exec, s[40:41]
	v_pk_fma_f32 v[14:15], v[14:15], v[18:19], v[144:145] op_sel_hi:[1,0,1]
	s_cbranch_vccnz .LBB0_616
	v_mov_b32_e32 v210, 0x3dd2d3e7
	v_pk_mul_f32 v[206:207], v[14:15], v[14:15]
	v_pk_mul_f32 v[208:209], v[16:17], v[16:17]
	v_pk_fma_f32 v[206:207], v[206:207], v[210:211], v[236:237] op_sel_hi:[1,0,0]
	v_pk_fma_f32 v[208:209], v[208:209], v[210:211], v[236:237] op_sel_hi:[1,0,0]
	v_pk_mul_f32 v[206:207], v[14:15], v[206:207]
	v_pk_mul_f32 v[208:209], v[16:17], v[208:209]
	v_exp_f32_e32 v206, v206
	v_exp_f32_e32 v207, v207
	v_exp_f32_e32 v208, v208
	v_exp_f32_e32 v209, v209
	v_pk_add_f32 v[206:207], v[206:207], 1.0 op_sel_hi:[1,0]
	v_pk_add_f32 v[208:209], v[208:209], 1.0 op_sel_hi:[1,0]
	v_rcp_f32_e32 v206, v206
	v_rcp_f32_e32 v207, v207
	v_rcp_f32_e32 v208, v208
	v_rcp_f32_e32 v209, v209
	v_pk_fma_f32 v[14:15], v[14:15], v[206:207], v[14:15] neg_lo:[1,0,0] neg_hi:[1,0,0]
	v_pk_fma_f32 v[16:17], v[16:17], v[208:209], v[16:17] neg_lo:[1,0,0] neg_hi:[1,0,0]
; __device__ __forceinline__ void store_bf16x8_wt(bf16* p, const f32x4 v0, const f32x4 v1) { u32x4 w; w.x = cvt_pk_bf16(v0[0], v0[1]); w.y = cvt_pk_bf16(v0[2], v0[3]); w.z = cvt_pk_bf16(v1[0], v1[1]); w.w = cvt_pk_bf16(v1[2], v1[3]); stg16_wt(p, w); }
; __device__ __forceinline__ float gelu_tanh(float x) {
;     const float C0 = 2.f * 0.7978845608028654f * L2E, C1 = 2.f * 0.7978845608028654f * 0.044715f * L2E;
;     const float e = __builtin_amdgcn_exp2f(x * __builtin_fmaf(x * x, C1, C0));
;     return __builtin_fmaf(-x, __builtin_amdgcn_rcpf(1.f + e), x);
; }
; template <bool FP8>
; __device__ __forceinline__ void epilogue(const Desc& d, const Acc& acc, const Tile& u, LAS unsigned char* lds) {
;     ...
;         for (int ai = 0; ai < 2; ++ai)
; #pragma unroll
;             for (int m = 0; m < 4; ++m)
; #pragma unroll
;                 for (int bj = 0; bj < 2; ++bj) { f32x4 v[2];
; #pragma unroll
;                     for (int n = 0; n < 2; ++n) { v[n] = acc[ai][bj][m][n] * rs[ai][m] + bv[bj][n];
;                         if (isg) { v[n][0] = gelu_tanh(v[n][0]); v[n][1] = gelu_tanh(v[n][1]); v[n][2] = gelu_tanh(v[n][2]); v[n][3] = gelu_tanh(v[n][3]); } }
;                     store_bf16x8_wt(O + (size_t)(row0 + ai * 128 + m * 16) * D + oc0 + bj * 128, v[0], v[1]); }
.LBB0_616:
	v_mov_b32_e32 v19, v18
	v_mov_b32_e32 v20, v18
	v_mov_b32_e32 v21, v18
	v_pk_fma_f32 v[12:13], v[12:13], v[20:21], v[142:143]
	s_and_b64 vcc, exec, s[40:41]
	v_pk_fma_f32 v[22:23], v[10:11], v[18:19], v[140:141]
	s_cbranch_vccnz .LBB0_618
	v_mov_b32_e32 v210, 0x3dd2d3e7
	v_pk_mul_f32 v[206:207], v[22:23], v[22:23]
	v_pk_mul_f32 v[208:209], v[12:13], v[12:13]
	v_pk_fma_f32 v[206:207], v[206:207], v[210:211], v[236:237] op_sel_hi:[1,0,0]
	v_pk_fma_f32 v[208:209], v[208:209], v[210:211], v[236:237] op_sel_hi:[1,0,0]
	v_pk_mul_f32 v[206:207], v[22:23], v[206:207]
	v_pk_mul_f32 v[208:209], v[12:13], v[208:209]
	v_exp_f32_e32 v206, v206
	v_exp_f32_e32 v207, v207
	v_exp_f32_e32 v208, v208
	v_exp_f32_e32 v209, v209
	v_pk_add_f32 v[206:207], v[206:207], 1.0 op_sel_hi:[1,0]
	v_pk_add_f32 v[208:209], v[208:209], 1.0 op_sel_hi:[1,0]
	v_rcp_f32_e32 v206, v206
	v_rcp_f32_e32 v207, v207
	v_rcp_f32_e32 v208, v208
	v_rcp_f32_e32 v209, v209
	v_pk_fma_f32 v[22:23], v[22:23], v[206:207], v[22:23] neg_lo:[1,0,0] neg_hi:[1,0,0]
	v_pk_fma_f32 v[12:13], v[12:13], v[208:209], v[12:13] neg_lo:[1,0,0] neg_hi:[1,0,0]
.LBB0_618:
	v_lshlrev_b64 v[10:11], 11, v[148:149]
	v_lshl_add_u64 v[10:11], v[124:125], 0, v[10:11]
	v_cvt_pk_bf16_f32 v14, v14, v15
	v_cvt_pk_bf16_f32 v15, v16, v17
	v_cvt_pk_bf16_f32 v16, v22, v23
	v_cvt_pk_bf16_f32 v17, v12, v13
	v_pk_fma_f32 v[8:9], v[8:9], v[20:21], v[138:139]
	global_store_dwordx4 v[10:11], v[14:17], off sc1
	s_nop 1
	s_and_b64 vcc, exec, s[40:41]
	v_pk_fma_f32 v[6:7], v[6:7], v[18:19], v[136:137]
	s_cbranch_vccnz .LBB0_620
	v_mov_b32_e32 v210, 0x3dd2d3e7
	v_pk_mul_f32 v[206:207], v[6:7], v[6:7]
	v_pk_mul_f32 v[208:209], v[8:9], v[8:9]
	v_pk_fma_f32 v[206:207], v[206:207], v[210:211], v[236:237] op_sel_hi:[1,0,0]
	v_pk_fma_f32 v[208:209], v[208:209], v[210:211], v[236:237] op_sel_hi:[1,0,0]
	v_pk_mul_f32 v[206:207], v[6:7], v[206:207]
	v_pk_mul_f32 v[208:209], v[8:9], v[208:209]
	v_exp_f32_e32 v206, v206
	v_exp_f32_e32 v207, v207
	v_exp_f32_e32 v208, v208
	v_exp_f32_e32 v209, v209
	v_pk_add_f32 v[206:207], v[206:207], 1.0 op_sel_hi:[1,0]
	v_pk_add_f32 v[208:209], v[208:209], 1.0 op_sel_hi:[1,0]
	v_rcp_f32_e32 v206, v206
	v_rcp_f32_e32 v207, v207
	v_rcp_f32_e32 v208, v208
	v_rcp_f32_e32 v209, v209
	v_pk_fma_f32 v[6:7], v[6:7], v[206:207], v[6:7] neg_lo:[1,0,0] neg_hi:[1,0,0]
	v_pk_fma_f32 v[8:9], v[8:9], v[208:209], v[8:9] neg_lo:[1,0,0] neg_hi:[1,0,0]
.LBB0_620:
	v_mov_b32_e32 v12, v18
	v_mov_b32_e32 v13, v18
	v_pk_fma_f32 v[4:5], v[4:5], v[12:13], v[134:135]
	s_and_b64 vcc, exec, s[40:41]
	v_pk_fma_f32 v[2:3], v[2:3], v[18:19], v[132:133]
	s_cbranch_vccnz .LBB0_622
	v_mov_b32_e32 v210, 0x3dd2d3e7
	v_pk_mul_f32 v[206:207], v[2:3], v[2:3]
	v_pk_mul_f32 v[208:209], v[4:5], v[4:5]
	v_pk_fma_f32 v[206:207], v[206:207], v[210:211], v[236:237] op_sel_hi:[1,0,0]
	v_pk_fma_f32 v[208:209], v[208:209], v[210:211], v[236:237] op_sel_hi:[1,0,0]
	v_pk_mul_f32 v[206:207], v[2:3], v[206:207]
	v_pk_mul_f32 v[208:209], v[4:5], v[208:209]
	v_exp_f32_e32 v206, v206
	v_exp_f32_e32 v207, v207
	v_exp_f32_e32 v208, v208
	v_exp_f32_e32 v209, v209
	v_pk_add_f32 v[206:207], v[206:207], 1.0 op_sel_hi:[1,0]
	v_pk_add_f32 v[208:209], v[208:209], 1.0 op_sel_hi:[1,0]
	v_rcp_f32_e32 v206, v206
	v_rcp_f32_e32 v207, v207
	v_rcp_f32_e32 v208, v208
	v_rcp_f32_e32 v209, v209
	v_pk_fma_f32 v[2:3], v[2:3], v[206:207], v[2:3] neg_lo:[1,0,0] neg_hi:[1,0,0]
	v_pk_fma_f32 v[4:5], v[4:5], v[208:209], v[4:5] neg_lo:[1,0,0] neg_hi:[1,0,0]
